# out_kernel body rewritten by hand: 16-byte global loads and ds_write_b128 staging (3 loads per chunk instead of 6 8-byte loads), 3 chunks in flight, same LDS layout and MFMA/accumulation order
# baseline (speedup 1.0000x reference)
_Z10out_kernelPKDF16_S0_PKfPf:
	s_load_dwordx8 s[4:11], s[0:1], 0x0
	s_lshr_b32 s12, s2, 3
	s_and_b32 s13, s2, 7
	s_lshl_b32 s14, s12, 5
	s_lshl_b32 s15, s13, 6
	v_lshrrev_b32_e32 v1, 3, v0
	v_and_b32_e32 v2, 7, v0
	v_lshlrev_b32_e32 v4, 4, v2
	v_add_u32_e32 v3, s14, v1
	v_lshl_or_b32 v3, v3, 10, v4
	v_add_u32_e32 v5, s15, v1
	v_lshl_or_b32 v5, v5, 10, v4
	v_add_u32_e32 v6, 0x8000, v5
	v_mul_u32_u24_e32 v7, 0x90, v1
	v_add_u32_e32 v7, v7, v4
	v_and_b32_e32 v8, 15, v0
	v_and_b32_e32 v9, 48, v0
	v_lshrrev_b32_e32 v10, 6, v0
	v_mul_u32_u24_e32 v11, 0x90, v8
	v_add_u32_e32 v11, v11, v9
	v_mul_u32_u24_e32 v12, 0x900, v10
	v_add_u32_e32 v12, v12, v11
	v_lshl_add_u32 v14, v10, 4, v8
	v_add_u32_e32 v14, s15, v14
	v_lshlrev_b32_e32 v15, 2, v14
	v_lshrrev_b32_e32 v13, 2, v9
	v_add_u32_e32 v13, s14, v13
	v_lshl_add_u32 v13, v13, 9, v14
	v_lshlrev_b32_e32 v16, 2, v13
	v_add_u32_e32 v17, 0x1000, v16
	v_add_u32_e32 v18, 0x8000, v16
	v_add_u32_e32 v19, 0x9000, v16
	s_waitcnt lgkmcnt(0)
	global_load_dwordx4 v[24:27], v3, s[4:5]
	global_load_dwordx4 v[28:31], v5, s[6:7]
	global_load_dwordx4 v[32:35], v6, s[6:7]
	global_load_dwordx4 v[36:39], v3, s[4:5] offset:128
	global_load_dwordx4 v[40:43], v5, s[6:7] offset:128
	global_load_dwordx4 v[44:47], v6, s[6:7] offset:128
	global_load_dwordx4 v[48:51], v3, s[4:5] offset:256
	global_load_dwordx4 v[52:55], v5, s[6:7] offset:256
	global_load_dwordx4 v[56:59], v6, s[6:7] offset:256
	global_load_dword v20, v15, s[8:9]
	s_waitcnt vmcnt(7)
	ds_write_b128 v7, v[24:27] offset:18432
	ds_write_b128 v7, v[28:31]
	ds_write_b128 v7, v[32:35] offset:4608
	global_load_dwordx4 v[24:27], v3, s[4:5] offset:384
	global_load_dwordx4 v[28:31], v5, s[6:7] offset:384
	global_load_dwordx4 v[32:35], v6, s[6:7] offset:384
	s_waitcnt lgkmcnt(0)
	s_barrier
	ds_read_b128 v[60:63], v11 offset:18432
	ds_read_b128 v[76:79], v12
	ds_read_b128 v[68:71], v11 offset:20736
	ds_read_b128 v[64:67], v11 offset:18496
	ds_read_b128 v[80:83], v12 offset:64
	ds_read_b128 v[72:75], v11 offset:20800
	s_waitcnt lgkmcnt(4)
	v_mfma_f32_16x16x32_f16 a[0:3], v[60:63], v[76:79], 0
	s_waitcnt lgkmcnt(3)
	v_mfma_f32_16x16x32_f16 a[4:7], v[68:71], v[76:79], 0
	s_waitcnt lgkmcnt(1)
	v_mfma_f32_16x16x32_f16 a[0:3], v[64:67], v[80:83], a[0:3]
	s_waitcnt lgkmcnt(0)
	v_mfma_f32_16x16x32_f16 a[4:7], v[72:75], v[80:83], a[4:7]
	s_waitcnt vmcnt(7)
	ds_write_b128 v7, v[36:39] offset:23040
	ds_write_b128 v7, v[40:43] offset:9216
	ds_write_b128 v7, v[44:47] offset:13824
	global_load_dwordx4 v[36:39], v3, s[4:5] offset:512
	global_load_dwordx4 v[40:43], v5, s[6:7] offset:512
	global_load_dwordx4 v[44:47], v6, s[6:7] offset:512
	s_waitcnt lgkmcnt(0)
	s_barrier
	ds_read_b128 v[60:63], v11 offset:23040
	ds_read_b128 v[76:79], v12 offset:9216
	ds_read_b128 v[68:71], v11 offset:25344
	ds_read_b128 v[64:67], v11 offset:23104
	ds_read_b128 v[80:83], v12 offset:9280
	ds_read_b128 v[72:75], v11 offset:25408
	s_waitcnt lgkmcnt(4)
	v_mfma_f32_16x16x32_f16 a[0:3], v[60:63], v[76:79], a[0:3]
	s_waitcnt lgkmcnt(3)
	v_mfma_f32_16x16x32_f16 a[4:7], v[68:71], v[76:79], a[4:7]
	s_waitcnt lgkmcnt(1)
	v_mfma_f32_16x16x32_f16 a[0:3], v[64:67], v[80:83], a[0:3]
	s_waitcnt lgkmcnt(0)
	v_mfma_f32_16x16x32_f16 a[4:7], v[72:75], v[80:83], a[4:7]
	s_waitcnt vmcnt(7)
	ds_write_b128 v7, v[48:51] offset:18432
	ds_write_b128 v7, v[52:55]
	ds_write_b128 v7, v[56:59] offset:4608
	global_load_dwordx4 v[48:51], v3, s[4:5] offset:640
	global_load_dwordx4 v[52:55], v5, s[6:7] offset:640
	global_load_dwordx4 v[56:59], v6, s[6:7] offset:640
	s_waitcnt lgkmcnt(0)
	s_barrier
	ds_read_b128 v[60:63], v11 offset:18432
	ds_read_b128 v[76:79], v12
	ds_read_b128 v[68:71], v11 offset:20736
	ds_read_b128 v[64:67], v11 offset:18496
	ds_read_b128 v[80:83], v12 offset:64
	ds_read_b128 v[72:75], v11 offset:20800
	s_waitcnt lgkmcnt(4)
	v_mfma_f32_16x16x32_f16 a[0:3], v[60:63], v[76:79], a[0:3]
	s_waitcnt lgkmcnt(3)
	v_mfma_f32_16x16x32_f16 a[4:7], v[68:71], v[76:79], a[4:7]
	s_waitcnt lgkmcnt(1)
	v_mfma_f32_16x16x32_f16 a[0:3], v[64:67], v[80:83], a[0:3]
	s_waitcnt lgkmcnt(0)
	v_mfma_f32_16x16x32_f16 a[4:7], v[72:75], v[80:83], a[4:7]
	s_waitcnt vmcnt(6)
	ds_write_b128 v7, v[24:27] offset:23040
	ds_write_b128 v7, v[28:31] offset:9216
	ds_write_b128 v7, v[32:35] offset:13824
	global_load_dwordx4 v[24:27], v3, s[4:5] offset:768
	global_load_dwordx4 v[28:31], v5, s[6:7] offset:768
	global_load_dwordx4 v[32:35], v6, s[6:7] offset:768
	s_waitcnt lgkmcnt(0)
	s_barrier
	ds_read_b128 v[60:63], v11 offset:23040
	ds_read_b128 v[76:79], v12 offset:9216
	ds_read_b128 v[68:71], v11 offset:25344
	ds_read_b128 v[64:67], v11 offset:23104
	ds_read_b128 v[80:83], v12 offset:9280
	ds_read_b128 v[72:75], v11 offset:25408
	s_waitcnt lgkmcnt(4)
	v_mfma_f32_16x16x32_f16 a[0:3], v[60:63], v[76:79], a[0:3]
	s_waitcnt lgkmcnt(3)
	v_mfma_f32_16x16x32_f16 a[4:7], v[68:71], v[76:79], a[4:7]
	s_waitcnt lgkmcnt(1)
	v_mfma_f32_16x16x32_f16 a[0:3], v[64:67], v[80:83], a[0:3]
	s_waitcnt lgkmcnt(0)
	v_mfma_f32_16x16x32_f16 a[4:7], v[72:75], v[80:83], a[4:7]
	s_waitcnt vmcnt(6)
	ds_write_b128 v7, v[36:39] offset:18432
	ds_write_b128 v7, v[40:43]
	ds_write_b128 v7, v[44:47] offset:4608
	global_load_dwordx4 v[36:39], v3, s[4:5] offset:896
	global_load_dwordx4 v[40:43], v5, s[6:7] offset:896
	global_load_dwordx4 v[44:47], v6, s[6:7] offset:896
	s_waitcnt lgkmcnt(0)
	s_barrier
	ds_read_b128 v[60:63], v11 offset:18432
	ds_read_b128 v[76:79], v12
	ds_read_b128 v[68:71], v11 offset:20736
	ds_read_b128 v[64:67], v11 offset:18496
	ds_read_b128 v[80:83], v12 offset:64
	ds_read_b128 v[72:75], v11 offset:20800
	s_waitcnt lgkmcnt(4)
	v_mfma_f32_16x16x32_f16 a[0:3], v[60:63], v[76:79], a[0:3]
	s_waitcnt lgkmcnt(3)
	v_mfma_f32_16x16x32_f16 a[4:7], v[68:71], v[76:79], a[4:7]
	s_waitcnt lgkmcnt(1)
	v_mfma_f32_16x16x32_f16 a[0:3], v[64:67], v[80:83], a[0:3]
	s_waitcnt lgkmcnt(0)
	v_mfma_f32_16x16x32_f16 a[4:7], v[72:75], v[80:83], a[4:7]
	s_waitcnt vmcnt(6)
	ds_write_b128 v7, v[48:51] offset:23040
	ds_write_b128 v7, v[52:55] offset:9216
	ds_write_b128 v7, v[56:59] offset:13824
	s_waitcnt lgkmcnt(0)
	s_barrier
	ds_read_b128 v[60:63], v11 offset:23040
	ds_read_b128 v[76:79], v12 offset:9216
	ds_read_b128 v[68:71], v11 offset:25344
	ds_read_b128 v[64:67], v11 offset:23104
	ds_read_b128 v[80:83], v12 offset:9280
	ds_read_b128 v[72:75], v11 offset:25408
	s_waitcnt lgkmcnt(4)
	v_mfma_f32_16x16x32_f16 a[0:3], v[60:63], v[76:79], a[0:3]
	s_waitcnt lgkmcnt(3)
	v_mfma_f32_16x16x32_f16 a[4:7], v[68:71], v[76:79], a[4:7]
	s_waitcnt lgkmcnt(1)
	v_mfma_f32_16x16x32_f16 a[0:3], v[64:67], v[80:83], a[0:3]
	s_waitcnt lgkmcnt(0)
	v_mfma_f32_16x16x32_f16 a[4:7], v[72:75], v[80:83], a[4:7]
	s_waitcnt vmcnt(3)
	ds_write_b128 v7, v[24:27] offset:18432
	ds_write_b128 v7, v[28:31]
	ds_write_b128 v7, v[32:35] offset:4608
	s_waitcnt lgkmcnt(0)
	s_barrier
	ds_read_b128 v[60:63], v11 offset:18432
	ds_read_b128 v[76:79], v12
	ds_read_b128 v[68:71], v11 offset:20736
	ds_read_b128 v[64:67], v11 offset:18496
	ds_read_b128 v[80:83], v12 offset:64
	ds_read_b128 v[72:75], v11 offset:20800
	s_waitcnt lgkmcnt(4)
	v_mfma_f32_16x16x32_f16 a[0:3], v[60:63], v[76:79], a[0:3]
	s_waitcnt lgkmcnt(3)
	v_mfma_f32_16x16x32_f16 a[4:7], v[68:71], v[76:79], a[4:7]
	s_waitcnt lgkmcnt(1)
	v_mfma_f32_16x16x32_f16 a[0:3], v[64:67], v[80:83], a[0:3]
	s_waitcnt lgkmcnt(0)
	v_mfma_f32_16x16x32_f16 a[4:7], v[72:75], v[80:83], a[4:7]
	s_waitcnt vmcnt(0)
	ds_write_b128 v7, v[36:39] offset:23040
	ds_write_b128 v7, v[40:43] offset:9216
	ds_write_b128 v7, v[44:47] offset:13824
	s_waitcnt lgkmcnt(0)
	s_barrier
	ds_read_b128 v[60:63], v11 offset:23040
	ds_read_b128 v[76:79], v12 offset:9216
	ds_read_b128 v[68:71], v11 offset:25344
	ds_read_b128 v[64:67], v11 offset:23104
	ds_read_b128 v[80:83], v12 offset:9280
	ds_read_b128 v[72:75], v11 offset:25408
	s_waitcnt lgkmcnt(4)
	v_mfma_f32_16x16x32_f16 a[0:3], v[60:63], v[76:79], a[0:3]
	s_waitcnt lgkmcnt(3)
	v_mfma_f32_16x16x32_f16 a[4:7], v[68:71], v[76:79], a[4:7]
	s_waitcnt lgkmcnt(1)
	v_mfma_f32_16x16x32_f16 a[0:3], v[64:67], v[80:83], a[0:3]
	s_waitcnt lgkmcnt(0)
	v_mfma_f32_16x16x32_f16 a[4:7], v[72:75], v[80:83], a[4:7]
	s_nop 7
	v_accvgpr_read_b32 v60, a0
	v_accvgpr_read_b32 v61, a1
	v_accvgpr_read_b32 v62, a2
	v_accvgpr_read_b32 v63, a3
	v_accvgpr_read_b32 v64, a4
	v_accvgpr_read_b32 v65, a5
	v_accvgpr_read_b32 v66, a6
	v_accvgpr_read_b32 v67, a7
	v_add_f32_e32 v60, v20, v60
	v_add_f32_e32 v61, v20, v61
	v_add_f32_e32 v62, v20, v62
	v_add_f32_e32 v63, v20, v63
	v_add_f32_e32 v64, v20, v64
	v_add_f32_e32 v65, v20, v65
	v_add_f32_e32 v66, v20, v66
	v_add_f32_e32 v67, v20, v67
	global_store_dword v16, v60, s[10:11]
	global_store_dword v16, v61, s[10:11] offset:2048
	global_store_dword v17, v62, s[10:11]
	global_store_dword v17, v63, s[10:11] offset:2048
	global_store_dword v18, v64, s[10:11]
	global_store_dword v18, v65, s[10:11] offset:2048
	global_store_dword v19, v66, s[10:11]
	global_store_dword v19, v67, s[10:11] offset:2048
	s_endpgm

	.amdhsa_kernel _Z10out_kernelPKDF16_S0_PKfPf
		.amdhsa_group_segment_fixed_size 27648
		.amdhsa_private_segment_fixed_size 0
		.amdhsa_kernarg_size 32
		.amdhsa_user_sgpr_count 2
		.amdhsa_user_sgpr_dispatch_ptr 0
		.amdhsa_user_sgpr_queue_ptr 0
		.amdhsa_user_sgpr_kernarg_segment_ptr 1
		.amdhsa_user_sgpr_dispatch_id 0
		.amdhsa_user_sgpr_kernarg_preload_length 0
		.amdhsa_user_sgpr_kernarg_preload_offset 0
		.amdhsa_user_sgpr_private_segment_size 0
		.amdhsa_uses_dynamic_stack 0
		.amdhsa_enable_private_segment 0
		.amdhsa_system_sgpr_workgroup_id_x 1
		.amdhsa_system_sgpr_workgroup_id_y 0
		.amdhsa_system_sgpr_workgroup_id_z 0
		.amdhsa_system_sgpr_workgroup_info 0
		.amdhsa_system_vgpr_workitem_id 0
		.amdhsa_next_free_vgpr 96
		.amdhsa_next_free_sgpr 96
		.amdhsa_accum_offset 84
		.amdhsa_reserve_vcc 1
		.amdhsa_float_round_mode_32 0
		.amdhsa_float_round_mode_16_64 0
		.amdhsa_float_denorm_mode_32 3
		.amdhsa_float_denorm_mode_16_64 3
		.amdhsa_dx10_clamp 1
		.amdhsa_ieee_mode 1
		.amdhsa_fp16_overflow 0
		.amdhsa_tg_split 0
		.amdhsa_exception_fp_ieee_invalid_op 0
		.amdhsa_exception_fp_denorm_src 0
		.amdhsa_exception_fp_ieee_div_zero 0
		.amdhsa_exception_fp_ieee_overflow 0
		.amdhsa_exception_fp_ieee_underflow 0
		.amdhsa_exception_fp_ieee_inexact 0
		.amdhsa_exception_int_div_zero 0
	.end_amdhsa_kernel

amdhsa.kernels:
  - .agpr_count:     0
    .args:
      - .actual_access:  read_only
        .address_space:  global
        .offset:         0
        .size:           8
        .value_kind:     global_buffer
      - .actual_access:  read_only
        .address_space:  global
        .offset:         8
        .size:           8
        .value_kind:     global_buffer
      - .actual_access:  read_only
        .address_space:  global
        .offset:         16
        .size:           8
        .value_kind:     global_buffer
      - .actual_access:  read_only
        .address_space:  global
        .offset:         24
        .size:           8
        .value_kind:     global_buffer
      - .address_space:  global
        .offset:         32
        .size:           8
        .value_kind:     global_buffer
      - .actual_access:  read_only
        .address_space:  global
        .offset:         40
        .size:           8
        .value_kind:     global_buffer
      - .address_space:  global
        .offset:         48
        .size:           8
        .value_kind:     global_buffer
      - .actual_access:  read_only
        .address_space:  global
        .offset:         56
        .size:           8
        .value_kind:     global_buffer
      - .address_space:  global
        .offset:         64
        .size:           8
        .value_kind:     global_buffer
      - .address_space:  global
        .offset:         72
        .size:           8
        .value_kind:     global_buffer
      - .address_space:  global
        .offset:         80
        .size:           8
        .value_kind:     global_buffer
      - .address_space:  global
        .offset:         88
        .size:           8
        .value_kind:     global_buffer
      - .address_space:  global
        .offset:         96
        .size:           8
        .value_kind:     global_buffer
      - .actual_access:  write_only
        .address_space:  global
        .offset:         104
        .size:           8
        .value_kind:     global_buffer
      - .actual_access:  write_only
        .address_space:  global
        .offset:         112
        .size:           8
        .value_kind:     global_buffer
      - .actual_access:  write_only
        .address_space:  global
        .offset:         120
        .size:           8
        .value_kind:     global_buffer
      - .actual_access:  write_only
        .address_space:  global
        .offset:         128
        .size:           8
        .value_kind:     global_buffer
      - .address_space:  global
        .offset:         136
        .size:           8
        .value_kind:     global_buffer
      - .address_space:  global
        .offset:         144
        .size:           8
        .value_kind:     global_buffer
      - .actual_access:  write_only
        .address_space:  global
        .offset:         152
        .size:           8
        .value_kind:     global_buffer
    .group_segment_fixed_size: 46112
    .kernarg_segment_align: 8
    .kernarg_segment_size: 160
    .language:       OpenCL C
    .language_version:
      - 2
      - 0
    .max_flat_workgroup_size: 512
    .name:           _Z11proj_kernelPKfS0_S0_S0_S0_S0_S0_S0_S0_S0_S0_S0_S0_PfS1_PDF16_S1_S0_S0_S2_
    .private_segment_fixed_size: 0
    .sgpr_count:     33
    .sgpr_spill_count: 0
    .symbol:         _Z11proj_kernelPKfS0_S0_S0_S0_S0_S0_S0_S0_S0_S0_S0_S0_PfS1_PDF16_S1_S0_S0_S2_.kd
    .uniform_work_group_size: 1
    .uses_dynamic_stack: false
    .vgpr_count:     133
    .vgpr_spill_count: 0
    .wavefront_size: 64
  - .agpr_count:     0
    .args:
      - .actual_access:  read_only
        .address_space:  global
        .offset:         0
        .size:           8
        .value_kind:     global_buffer
      - .actual_access:  read_only
        .address_space:  global
        .offset:         8
        .size:           8
        .value_kind:     global_buffer
      - .actual_access:  read_only
        .address_space:  global
        .offset:         16
        .size:           8
        .value_kind:     global_buffer
      - .actual_access:  read_only
        .address_space:  global
        .offset:         24
        .size:           8
        .value_kind:     global_buffer
      - .actual_access:  read_only
        .address_space:  global
        .offset:         32
        .size:           8
        .value_kind:     global_buffer
      - .actual_access:  read_only
        .address_space:  global
        .offset:         40
        .size:           8
        .value_kind:     global_buffer
      - .actual_access:  read_only
        .address_space:  global
        .offset:         48
        .size:           8
        .value_kind:     global_buffer
      - .actual_access:  write_only
        .address_space:  global
        .offset:         56
        .size:           8
        .value_kind:     global_buffer
      - .actual_access:  write_only
        .address_space:  global
        .offset:         64
        .size:           8
        .value_kind:     global_buffer
    .group_segment_fixed_size: 0
    .kernarg_segment_align: 8
    .kernarg_segment_size: 72
    .language:       OpenCL C
    .language_version:
      - 2
      - 0
    .max_flat_workgroup_size: 768
    .name:           _Z11attn_kernelPKfS0_PKDF16_S0_S0_S0_S2_PDF16_S3_
    .private_segment_fixed_size: 0
    .sgpr_count:     70
    .sgpr_spill_count: 0
    .symbol:         _Z11attn_kernelPKfS0_PKDF16_S0_S0_S0_S2_PDF16_S3_.kd
    .uniform_work_group_size: 1
    .uses_dynamic_stack: false
    .vgpr_count:     168
    .vgpr_spill_count: 0
    .wavefront_size: 64
  - .agpr_count:     8
    .args:
      - .actual_access:  read_only
        .address_space:  global
        .offset:         0
        .size:           8
        .value_kind:     global_buffer
      - .actual_access:  read_only
        .address_space:  global
        .offset:         8
        .size:           8
        .value_kind:     global_buffer
      - .actual_access:  read_only
        .address_space:  global
        .offset:         16
        .size:           8
        .value_kind:     global_buffer
      - .actual_access:  write_only
        .address_space:  global
        .offset:         24
        .size:           8
        .value_kind:     global_buffer
    .group_segment_fixed_size: 27648
    .kernarg_segment_align: 8
    .kernarg_segment_size: 32
    .language:       OpenCL C
    .language_version:
      - 2
      - 0
    .max_flat_workgroup_size: 256
    .name:           _Z10out_kernelPKDF16_S0_PKfPf
    .private_segment_fixed_size: 0
    .sgpr_count:     18
    .sgpr_spill_count: 0
    .symbol:         _Z10out_kernelPKDF16_S0_PKfPf.kd
    .uniform_work_group_size: 1
    .uses_dynamic_stack: false
    .vgpr_count:     96
    .vgpr_spill_count: 0
    .wavefront_size: 64
